# G2 epilogue layer-0 (f32 residual) path: residual loads pipelined two row groups deep
# baseline (speedup 1.0000x reference)
.LBB0_817:
	s_mul_hi_i32 s0, s53, 0x7e07e07f
	s_lshr_b32 s1, s0, 31
	s_ashr_i32 s0, s0, 5
	s_add_i32 s4, s0, s1
	s_mul_i32 s0, s4, 0xffffffbf
	s_sub_i32 s1, 0, s53
	s_mul_i32 s5, s4, 0x1800
	s_cmp_lg_u32 s0, s1
	s_cselect_b32 s0, s5, 0x3000
	s_ashr_i32 s1, s0, 31
	s_lshl_b64 s[0:1], s[0:1], 2
	s_add_u32 s0, s41, s0
	v_lshl_or_b32 v64, s54, 8, v174
	s_addc_u32 s1, s42, s1
	v_lshl_add_u64 v[70:71], v[64:65], 2, s[0:1]
	global_load_dwordx4 v[74:77], v[70:71], off offset:16
	global_load_dwordx4 v[78:81], v[70:71], off
	global_load_dwordx4 v[66:69], v[70:71], off offset:528
	s_nop 0
	global_load_dwordx4 v[70:73], v[70:71], off offset:512
	v_lshl_add_u32 v166, s53, 8, v172
	s_mul_i32 s27, s4, 0xffffbf00
	s_lshl_b32 s53, s4, 14
	s_addk_i32 s53, 0xff00
	s_lshl_b32 s26, s4, 8
	v_add_u32_e32 v148, s27, v166
	v_cmp_gt_i32_e64 s[0:1], s87, v148
	v_add_u32_e32 v146, s53, v148
	v_add_u32_e32 v148, s26, v148
	v_ashrrev_i32_e32 v147, 31, v146
	v_ashrrev_i32_e32 v149, 31, v148
	v_lshlrev_b64 v[146:147], 12, v[146:147]
	v_lshlrev_b64 v[148:149], 12, v[148:149]
	v_cndmask_b32_e64 v150, 0, 1, s[22:23]
	v_lshl_add_u64 v[148:149], s[6:7], 0, v[148:149]
	v_lshl_add_u64 v[146:147], s[8:9], 0, v[146:147]
	v_cmp_ne_u32_e64 s[4:5], 1, v150
	s_andn2_b64 vcc, exec, s[22:23]
	v_cndmask_b32_e64 v171, v147, v149, s[0:1]
	v_cndmask_b32_e64 v170, v146, v148, s[0:1]
	s_cbranch_vccnz .Lg2epi_fast
	s_branch .Lg2epi_fastA
	global_load_dwordx4 v[146:149], v[150:151], off offset:16
	s_nop 0
	global_load_dwordx4 v[150:153], v[150:151], off
	s_mov_b64 s[0:1], 0
	s_branch .LBB0_820
.Lg2epi_fastA:
	s_mov_b32 s100, 0x8000
	s_mov_b32 s101, 0
	v_ashrrev_i32_e32 v167, 31, v166
	v_lshlrev_b64 v[168:169], 11, v[166:167]
	v_lshl_add_u64 v[168:169], s[18:19], 0, v[168:169]
	v_lshlrev_b32_e32 v176, 1, v64
	v_mov_b32_e32 v177, v65
	v_lshl_add_u64 v[168:169], v[168:169], 0, v[176:177]
	v_mov_b64_e32 v[178:179], v[168:169]
	v_mov_b32_e32 v190, v166
	v_add_u32_e32 v190, s27, v190
	v_cmp_gt_i32_e64 s[0:1], s87, v190
	v_add_u32_e32 v192, s53, v190
	v_add_u32_e32 v194, s26, v190
	v_ashrrev_i32_e32 v193, 31, v192
	v_ashrrev_i32_e32 v195, 31, v194
	v_lshlrev_b64 v[192:193], 12, v[192:193]
	v_lshlrev_b64 v[194:195], 12, v[194:195]
	v_lshl_add_u64 v[194:195], s[6:7], 0, v[194:195]
	v_lshl_add_u64 v[192:193], s[8:9], 0, v[192:193]
	v_cndmask_b32_e64 v189, v193, v195, s[0:1]
	v_cndmask_b32_e64 v188, v192, v194, s[0:1]
	v_lshl_add_u64 v[188:189], v[64:65], 2, v[188:189]
	global_load_dwordx4 v[216:219], v[188:189], off offset:16
	global_load_dwordx4 v[212:215], v[188:189], off
	global_load_dwordx4 v[224:227], v[188:189], off offset:528
	global_load_dwordx4 v[220:223], v[188:189], off offset:512
	v_add_u32_e32 v190, 16, v166
	v_add_u32_e32 v190, s27, v190
	v_cmp_gt_i32_e64 s[0:1], s87, v190
	v_add_u32_e32 v192, s53, v190
	v_add_u32_e32 v194, s26, v190
	v_ashrrev_i32_e32 v193, 31, v192
	v_ashrrev_i32_e32 v195, 31, v194
	v_lshlrev_b64 v[192:193], 12, v[192:193]
	v_lshlrev_b64 v[194:195], 12, v[194:195]
	v_lshl_add_u64 v[194:195], s[6:7], 0, v[194:195]
	v_lshl_add_u64 v[192:193], s[8:9], 0, v[192:193]
	v_cndmask_b32_e64 v189, v193, v195, s[0:1]
	v_cndmask_b32_e64 v188, v192, v194, s[0:1]
	v_lshl_add_u64 v[188:189], v[64:65], 2, v[188:189]
	global_load_dwordx4 v[232:235], v[188:189], off offset:16
	global_load_dwordx4 v[228:231], v[188:189], off
	global_load_dwordx4 v[184:187], v[188:189], off offset:528
	global_load_dwordx4 v[180:183], v[188:189], off offset:512
	s_waitcnt vmcnt(4)
	v_pk_fma_f32 v[142:143], v[142:143], v[78:79], v[212:213]
	v_pk_fma_f32 v[144:145], v[144:145], v[80:81], v[214:215]
	v_pk_fma_f32 v[138:139], v[138:139], v[74:75], v[216:217]
	v_pk_fma_f32 v[140:141], v[140:141], v[76:77], v[218:219]
	v_cvt_pk_bf16_f32 v212, v142, v143
	v_cvt_pk_bf16_f32 v213, v144, v145
	v_cvt_pk_bf16_f32 v214, v138, v139
	v_cvt_pk_bf16_f32 v215, v140, v141
	global_store_dwordx4 v[178:179], v[212:215], off
	s_nop 1
	v_pk_fma_f32 v[134:135], v[134:135], v[70:71], v[220:221]
	v_pk_fma_f32 v[136:137], v[136:137], v[72:73], v[222:223]
	v_pk_fma_f32 v[130:131], v[130:131], v[66:67], v[224:225]
	v_pk_fma_f32 v[132:133], v[132:133], v[68:69], v[226:227]
	v_cvt_pk_bf16_f32 v220, v134, v135
	v_cvt_pk_bf16_f32 v221, v136, v137
	v_cvt_pk_bf16_f32 v222, v130, v131
	v_cvt_pk_bf16_f32 v223, v132, v133
	global_store_dwordx4 v[178:179], v[220:223], off offset:256
	v_lshl_add_u64 v[178:179], v[178:179], 0, s[100:101]
	v_add_u32_e32 v190, 32, v166
	v_add_u32_e32 v190, s27, v190
	v_cmp_gt_i32_e64 s[0:1], s87, v190
	v_add_u32_e32 v192, s53, v190
	v_add_u32_e32 v194, s26, v190
	v_ashrrev_i32_e32 v193, 31, v192
	v_ashrrev_i32_e32 v195, 31, v194
	v_lshlrev_b64 v[192:193], 12, v[192:193]
	v_lshlrev_b64 v[194:195], 12, v[194:195]
	v_lshl_add_u64 v[194:195], s[6:7], 0, v[194:195]
	v_lshl_add_u64 v[192:193], s[8:9], 0, v[192:193]
	v_cndmask_b32_e64 v189, v193, v195, s[0:1]
	v_cndmask_b32_e64 v188, v192, v194, s[0:1]
	v_lshl_add_u64 v[188:189], v[64:65], 2, v[188:189]
	global_load_dwordx4 v[216:219], v[188:189], off offset:16
	global_load_dwordx4 v[212:215], v[188:189], off
	global_load_dwordx4 v[224:227], v[188:189], off offset:528
	global_load_dwordx4 v[220:223], v[188:189], off offset:512
	s_waitcnt vmcnt(6)
	v_pk_fma_f32 v[126:127], v[126:127], v[78:79], v[228:229]
	v_pk_fma_f32 v[128:129], v[128:129], v[80:81], v[230:231]
	v_pk_fma_f32 v[122:123], v[122:123], v[74:75], v[232:233]
	v_pk_fma_f32 v[124:125], v[124:125], v[76:77], v[234:235]
	v_cvt_pk_bf16_f32 v228, v126, v127
	v_cvt_pk_bf16_f32 v229, v128, v129
	v_cvt_pk_bf16_f32 v230, v122, v123
	v_cvt_pk_bf16_f32 v231, v124, v125
	global_store_dwordx4 v[178:179], v[228:231], off
	s_nop 1
	v_pk_fma_f32 v[118:119], v[118:119], v[70:71], v[180:181]
	v_pk_fma_f32 v[120:121], v[120:121], v[72:73], v[182:183]
	v_pk_fma_f32 v[114:115], v[114:115], v[66:67], v[184:185]
	v_pk_fma_f32 v[116:117], v[116:117], v[68:69], v[186:187]
	v_cvt_pk_bf16_f32 v180, v118, v119
	v_cvt_pk_bf16_f32 v181, v120, v121
	v_cvt_pk_bf16_f32 v182, v114, v115
	v_cvt_pk_bf16_f32 v183, v116, v117
	global_store_dwordx4 v[178:179], v[180:183], off offset:256
	v_lshl_add_u64 v[178:179], v[178:179], 0, s[100:101]
	v_add_u32_e32 v190, 48, v166
	v_add_u32_e32 v190, s27, v190
	v_cmp_gt_i32_e64 s[0:1], s87, v190
	v_add_u32_e32 v192, s53, v190
	v_add_u32_e32 v194, s26, v190
	v_ashrrev_i32_e32 v193, 31, v192
	v_ashrrev_i32_e32 v195, 31, v194
	v_lshlrev_b64 v[192:193], 12, v[192:193]
	v_lshlrev_b64 v[194:195], 12, v[194:195]
	v_lshl_add_u64 v[194:195], s[6:7], 0, v[194:195]
	v_lshl_add_u64 v[192:193], s[8:9], 0, v[192:193]
	v_cndmask_b32_e64 v189, v193, v195, s[0:1]
	v_cndmask_b32_e64 v188, v192, v194, s[0:1]
	v_lshl_add_u64 v[188:189], v[64:65], 2, v[188:189]
	global_load_dwordx4 v[232:235], v[188:189], off offset:16
	global_load_dwordx4 v[228:231], v[188:189], off
	global_load_dwordx4 v[184:187], v[188:189], off offset:528
	global_load_dwordx4 v[180:183], v[188:189], off offset:512
	s_waitcnt vmcnt(6)
	v_pk_fma_f32 v[110:111], v[110:111], v[78:79], v[212:213]
	v_pk_fma_f32 v[112:113], v[112:113], v[80:81], v[214:215]
	v_pk_fma_f32 v[106:107], v[106:107], v[74:75], v[216:217]
	v_pk_fma_f32 v[108:109], v[108:109], v[76:77], v[218:219]
	v_cvt_pk_bf16_f32 v212, v110, v111
	v_cvt_pk_bf16_f32 v213, v112, v113
	v_cvt_pk_bf16_f32 v214, v106, v107
	v_cvt_pk_bf16_f32 v215, v108, v109
	global_store_dwordx4 v[178:179], v[212:215], off
	s_nop 1
	v_pk_fma_f32 v[102:103], v[102:103], v[70:71], v[220:221]
	v_pk_fma_f32 v[104:105], v[104:105], v[72:73], v[222:223]
	v_pk_fma_f32 v[98:99], v[98:99], v[66:67], v[224:225]
	v_pk_fma_f32 v[100:101], v[100:101], v[68:69], v[226:227]
	v_cvt_pk_bf16_f32 v220, v102, v103
	v_cvt_pk_bf16_f32 v221, v104, v105
	v_cvt_pk_bf16_f32 v222, v98, v99
	v_cvt_pk_bf16_f32 v223, v100, v101
	global_store_dwordx4 v[178:179], v[220:223], off offset:256
	v_lshl_add_u64 v[178:179], v[178:179], 0, s[100:101]
	v_add_u32_e32 v190, 128, v166
	v_add_u32_e32 v190, s27, v190
	v_cmp_gt_i32_e64 s[0:1], s87, v190
	v_add_u32_e32 v192, s53, v190
	v_add_u32_e32 v194, s26, v190
	v_ashrrev_i32_e32 v193, 31, v192
	v_ashrrev_i32_e32 v195, 31, v194
	v_lshlrev_b64 v[192:193], 12, v[192:193]
	v_lshlrev_b64 v[194:195], 12, v[194:195]
	v_lshl_add_u64 v[194:195], s[6:7], 0, v[194:195]
	v_lshl_add_u64 v[192:193], s[8:9], 0, v[192:193]
	v_cndmask_b32_e64 v189, v193, v195, s[0:1]
	v_cndmask_b32_e64 v188, v192, v194, s[0:1]
	v_lshl_add_u64 v[188:189], v[64:65], 2, v[188:189]
	global_load_dwordx4 v[216:219], v[188:189], off offset:16
	global_load_dwordx4 v[212:215], v[188:189], off
	global_load_dwordx4 v[224:227], v[188:189], off offset:528
	global_load_dwordx4 v[220:223], v[188:189], off offset:512
	s_waitcnt vmcnt(6)
	v_pk_fma_f32 v[94:95], v[94:95], v[78:79], v[228:229]
	v_pk_fma_f32 v[96:97], v[96:97], v[80:81], v[230:231]
	v_pk_fma_f32 v[90:91], v[90:91], v[74:75], v[232:233]
	v_pk_fma_f32 v[92:93], v[92:93], v[76:77], v[234:235]
	v_cvt_pk_bf16_f32 v228, v94, v95
	v_cvt_pk_bf16_f32 v229, v96, v97
	v_cvt_pk_bf16_f32 v230, v90, v91
	v_cvt_pk_bf16_f32 v231, v92, v93
	global_store_dwordx4 v[178:179], v[228:231], off
	s_nop 1
	v_pk_fma_f32 v[86:87], v[86:87], v[70:71], v[180:181]
	v_pk_fma_f32 v[88:89], v[88:89], v[72:73], v[182:183]
	v_pk_fma_f32 v[82:83], v[82:83], v[66:67], v[184:185]
	v_pk_fma_f32 v[84:85], v[84:85], v[68:69], v[186:187]
	v_cvt_pk_bf16_f32 v180, v86, v87
	v_cvt_pk_bf16_f32 v181, v88, v89
	v_cvt_pk_bf16_f32 v182, v82, v83
	v_cvt_pk_bf16_f32 v183, v84, v85
	global_store_dwordx4 v[178:179], v[180:183], off offset:256
	v_lshl_add_u64 v[178:179], s[100:101], 3, v[168:169]
	v_add_u32_e32 v190, 144, v166
	v_add_u32_e32 v190, s27, v190
	v_cmp_gt_i32_e64 s[0:1], s87, v190
	v_add_u32_e32 v192, s53, v190
	v_add_u32_e32 v194, s26, v190
	v_ashrrev_i32_e32 v193, 31, v192
	v_ashrrev_i32_e32 v195, 31, v194
	v_lshlrev_b64 v[192:193], 12, v[192:193]
	v_lshlrev_b64 v[194:195], 12, v[194:195]
	v_lshl_add_u64 v[194:195], s[6:7], 0, v[194:195]
	v_lshl_add_u64 v[192:193], s[8:9], 0, v[192:193]
	v_cndmask_b32_e64 v189, v193, v195, s[0:1]
	v_cndmask_b32_e64 v188, v192, v194, s[0:1]
	v_lshl_add_u64 v[188:189], v[64:65], 2, v[188:189]
	global_load_dwordx4 v[232:235], v[188:189], off offset:16
	global_load_dwordx4 v[228:231], v[188:189], off
	global_load_dwordx4 v[184:187], v[188:189], off offset:528
	global_load_dwordx4 v[180:183], v[188:189], off offset:512
	s_waitcnt vmcnt(6)
	v_pk_fma_f32 v[60:61], v[60:61], v[78:79], v[212:213]
	v_pk_fma_f32 v[62:63], v[62:63], v[80:81], v[214:215]
	v_pk_fma_f32 v[56:57], v[56:57], v[74:75], v[216:217]
	v_pk_fma_f32 v[58:59], v[58:59], v[76:77], v[218:219]
	v_cvt_pk_bf16_f32 v212, v60, v61
	v_cvt_pk_bf16_f32 v213, v62, v63
	v_cvt_pk_bf16_f32 v214, v56, v57
	v_cvt_pk_bf16_f32 v215, v58, v59
	global_store_dwordx4 v[178:179], v[212:215], off
	s_nop 1
	v_pk_fma_f32 v[52:53], v[52:53], v[70:71], v[220:221]
	v_pk_fma_f32 v[54:55], v[54:55], v[72:73], v[222:223]
	v_pk_fma_f32 v[48:49], v[48:49], v[66:67], v[224:225]
	v_pk_fma_f32 v[50:51], v[50:51], v[68:69], v[226:227]
	v_cvt_pk_bf16_f32 v220, v52, v53
	v_cvt_pk_bf16_f32 v221, v54, v55
	v_cvt_pk_bf16_f32 v222, v48, v49
	v_cvt_pk_bf16_f32 v223, v50, v51
	global_store_dwordx4 v[178:179], v[220:223], off offset:256
	v_lshl_add_u64 v[178:179], v[178:179], 0, s[100:101]
	v_add_u32_e32 v190, 160, v166
	v_add_u32_e32 v190, s27, v190
	v_cmp_gt_i32_e64 s[0:1], s87, v190
	v_add_u32_e32 v192, s53, v190
	v_add_u32_e32 v194, s26, v190
	v_ashrrev_i32_e32 v193, 31, v192
	v_ashrrev_i32_e32 v195, 31, v194
	v_lshlrev_b64 v[192:193], 12, v[192:193]
	v_lshlrev_b64 v[194:195], 12, v[194:195]
	v_lshl_add_u64 v[194:195], s[6:7], 0, v[194:195]
	v_lshl_add_u64 v[192:193], s[8:9], 0, v[192:193]
	v_cndmask_b32_e64 v189, v193, v195, s[0:1]
	v_cndmask_b32_e64 v188, v192, v194, s[0:1]
	v_lshl_add_u64 v[188:189], v[64:65], 2, v[188:189]
	global_load_dwordx4 v[216:219], v[188:189], off offset:16
	global_load_dwordx4 v[212:215], v[188:189], off
	global_load_dwordx4 v[224:227], v[188:189], off offset:528
	global_load_dwordx4 v[220:223], v[188:189], off offset:512
	s_waitcnt vmcnt(6)
	v_pk_fma_f32 v[44:45], v[44:45], v[78:79], v[228:229]
	v_pk_fma_f32 v[46:47], v[46:47], v[80:81], v[230:231]
	v_pk_fma_f32 v[40:41], v[40:41], v[74:75], v[232:233]
	v_pk_fma_f32 v[42:43], v[42:43], v[76:77], v[234:235]
	v_cvt_pk_bf16_f32 v228, v44, v45
	v_cvt_pk_bf16_f32 v229, v46, v47
	v_cvt_pk_bf16_f32 v230, v40, v41
	v_cvt_pk_bf16_f32 v231, v42, v43
	global_store_dwordx4 v[178:179], v[228:231], off
	s_nop 1
	v_pk_fma_f32 v[36:37], v[36:37], v[70:71], v[180:181]
	v_pk_fma_f32 v[38:39], v[38:39], v[72:73], v[182:183]
	v_pk_fma_f32 v[32:33], v[32:33], v[66:67], v[184:185]
	v_pk_fma_f32 v[34:35], v[34:35], v[68:69], v[186:187]
	v_cvt_pk_bf16_f32 v180, v36, v37
	v_cvt_pk_bf16_f32 v181, v38, v39
	v_cvt_pk_bf16_f32 v182, v32, v33
	v_cvt_pk_bf16_f32 v183, v34, v35
	global_store_dwordx4 v[178:179], v[180:183], off offset:256
	v_lshl_add_u64 v[178:179], v[178:179], 0, s[100:101]
	v_add_u32_e32 v190, 176, v166
	v_add_u32_e32 v190, s27, v190
	v_cmp_gt_i32_e64 s[0:1], s87, v190
	v_add_u32_e32 v192, s53, v190
	v_add_u32_e32 v194, s26, v190
	v_ashrrev_i32_e32 v193, 31, v192
	v_ashrrev_i32_e32 v195, 31, v194
	v_lshlrev_b64 v[192:193], 12, v[192:193]
	v_lshlrev_b64 v[194:195], 12, v[194:195]
	v_lshl_add_u64 v[194:195], s[6:7], 0, v[194:195]
	v_lshl_add_u64 v[192:193], s[8:9], 0, v[192:193]
	v_cndmask_b32_e64 v189, v193, v195, s[0:1]
	v_cndmask_b32_e64 v188, v192, v194, s[0:1]
	v_lshl_add_u64 v[188:189], v[64:65], 2, v[188:189]
	global_load_dwordx4 v[232:235], v[188:189], off offset:16
	global_load_dwordx4 v[228:231], v[188:189], off
	global_load_dwordx4 v[184:187], v[188:189], off offset:528
	global_load_dwordx4 v[180:183], v[188:189], off offset:512
	s_waitcnt vmcnt(6)
	v_pk_fma_f32 v[28:29], v[28:29], v[78:79], v[212:213]
	v_pk_fma_f32 v[30:31], v[30:31], v[80:81], v[214:215]
	v_pk_fma_f32 v[24:25], v[24:25], v[74:75], v[216:217]
	v_pk_fma_f32 v[26:27], v[26:27], v[76:77], v[218:219]
	v_cvt_pk_bf16_f32 v212, v28, v29
	v_cvt_pk_bf16_f32 v213, v30, v31
	v_cvt_pk_bf16_f32 v214, v24, v25
	v_cvt_pk_bf16_f32 v215, v26, v27
	global_store_dwordx4 v[178:179], v[212:215], off
	s_nop 1
	v_pk_fma_f32 v[20:21], v[20:21], v[70:71], v[220:221]
	v_pk_fma_f32 v[22:23], v[22:23], v[72:73], v[222:223]
	v_pk_fma_f32 v[16:17], v[16:17], v[66:67], v[224:225]
	v_pk_fma_f32 v[18:19], v[18:19], v[68:69], v[226:227]
	v_cvt_pk_bf16_f32 v220, v20, v21
	v_cvt_pk_bf16_f32 v221, v22, v23
	v_cvt_pk_bf16_f32 v222, v16, v17
	v_cvt_pk_bf16_f32 v223, v18, v19
	global_store_dwordx4 v[178:179], v[220:223], off offset:256
	v_lshl_add_u64 v[178:179], v[178:179], 0, s[100:101]
	s_waitcnt vmcnt(2)
	v_pk_fma_f32 v[12:13], v[12:13], v[78:79], v[228:229]
	v_pk_fma_f32 v[14:15], v[14:15], v[80:81], v[230:231]
	v_pk_fma_f32 v[8:9], v[8:9], v[74:75], v[232:233]
	v_pk_fma_f32 v[10:11], v[10:11], v[76:77], v[234:235]
	v_cvt_pk_bf16_f32 v228, v12, v13
	v_cvt_pk_bf16_f32 v229, v14, v15
	v_cvt_pk_bf16_f32 v230, v8, v9
	v_cvt_pk_bf16_f32 v231, v10, v11
	global_store_dwordx4 v[178:179], v[228:231], off
	s_nop 1
	v_pk_fma_f32 v[4:5], v[4:5], v[70:71], v[180:181]
	v_pk_fma_f32 v[6:7], v[6:7], v[72:73], v[182:183]
	v_pk_fma_f32 v[0:1], v[0:1], v[66:67], v[184:185]
	v_pk_fma_f32 v[2:3], v[2:3], v[68:69], v[186:187]
	v_cvt_pk_bf16_f32 v180, v4, v5
	v_cvt_pk_bf16_f32 v181, v6, v7
	v_cvt_pk_bf16_f32 v182, v0, v1
	v_cvt_pk_bf16_f32 v183, v2, v3
	global_store_dwordx4 v[178:179], v[180:183], off offset:256
	s_andn2_b64 vcc, exec, s[24:25]
	s_mov_b64 s[0:1], -1
	s_branch .Lg2epi_join
